# out-proj epilogue: bf16 t rows pass through a per-wave LDS image so each global_store_dwordx4 writes 8 full lines (as the in-proj epilogue)
# speedup vs baseline: 1.0262x; 1.0104x over previous
; #define LAS __attribute__((address_space(3)))
; __device__ __forceinline__ unsigned cvt_pk_bf16(float lo, float hi) { unsigned r; asm volatile("v_cvt_pk_bf16_f32 %0, %1, %2" : "=v"(r) : "v"(lo), "v"(hi)); return r; }
;     __device__ __forceinline__ void operator()(const f32x4 (&acc)[2][2][4][2], const Unit& u, int wr, int wc, int fr, int fq, const LAS unsigned* rt) const {
;         const int b = (u.pm * BM) >> 11; const int col0 = u.pn * BM + wc * 64 + 16 * fq;
;         f32x4 g[2][2];
; #pragma unroll
;         for (int bj = 0; bj < 2; ++bj)
; #pragma unroll
;             for (int n = 0; n < 2; ++n) g[bj][n] = *(const f32x4*)(mod + b * 6144 + MOD_GATE_A + col0 + 8 * bj + 4 * n) * INV_IN8;
; #pragma unroll
;         for (int ai = 0; ai < 2; ++ai)
; #pragma unroll
;             for (int m = 0; m < 4; ++m) { const size_t o = (size_t)(u.pm * BM + ai * HALF + wr * 64 + m * 16 + fr) * D + col0;
;                 const f32x4 x0 = *(const f32x4*)(x + o), x1 = *(const f32x4*)(x + o + 4), x2 = *(const f32x4*)(x + o + 8), x3 = *(const f32x4*)(x + o + 12);
;                 const f32x4 xs[2][2] = {{x0, x1}, {x2, x3}};
; #pragma unroll
;                 for (int bj = 0; bj < 2; ++bj) {
;                     const f32x4 t0 = xs[bj][0] * ALPHA + g[bj][0] * acc[ai][bj][m][0], t1 = xs[bj][1] * ALPHA + g[bj][1] * acc[ai][bj][m][1];
;                     u32x4 w; w.x = cvt_pk_bf16(t0[0], t0[1]); w.y = cvt_pk_bf16(t0[2], t0[3]); w.z = cvt_pk_bf16(t1[0], t1[1]); w.w = cvt_pk_bf16(t1[2], t1[3]);
;                     *(u32x4*)(tb + o + 8 * bj) = w; } }
.LBB0_409:
	s_lshl_b32 s100, s12, 18
	s_add_i32 s100, s100, s98
	s_bfe_u32 s100, s100, 0x20012
	s_lshr_b32 s4, s65, 3
	s_mulk_i32 s4, 0x1800
	s_ashr_i32 s5, s4, 31
	s_lshl_b64 s[4:5], s[4:5], 2
	v_lshl_add_u32 v16, s100, 8, v185
	s_add_u32 s4, s85, s4
	s_addc_u32 s5, s87, s5
	v_ashrrev_i32_e32 v17, 31, v16
	v_lshl_add_u64 v[0:1], v[16:17], 2, s[4:5]
	s_mov_b64 s[4:5], 0x2000
	v_lshl_add_u64 v[4:5], v[0:1], 0, s[4:5]
	v_add_co_u32_e32 v0, vcc, s41, v0
	s_nop 15
	s_nop 15
	s_nop 1
	v_addc_co_u32_e32 v1, vcc, 0, v1, vcc
	global_load_dwordx4 v[0:3], v[0:1], off
	s_nop 0
	global_load_dwordx4 v[18:21], v[4:5], off offset:48
	global_load_dwordx4 v[174:177], v[4:5], off offset:32
	s_nop 0
	global_load_dwordx4 v[4:7], v[4:5], off offset:16
	s_mov_b64 s[4:5], -1
	s_cmp_eq_u32 s13, 3
	v_lshl_add_u32 v192, s65, 8, v186
	v_ashrrev_i32_e32 v193, 31, v192
	v_lshlrev_b64 v[192:193], 10, v[192:193]
	v_lshl_add_u64 v[192:193], v[192:193], 0, v[16:17]
	v_mbcnt_lo_u32_b32 v26, -1, 0
	v_mbcnt_hi_u32_b32 v26, -1, v26
	v_and_b32_e32 v27, 7, v26
	v_and_b32_e32 v16, 0xffffffc0, v16
	v_lshl_or_b32 v16, v27, 3, v16
	v_lshrrev_b32_e32 v25, 3, v26
	v_mul_u32_u24_e32 v191, 0x90, v25
	v_lshl_add_u32 v191, v27, 4, v191
	v_and_b32_e32 v27, 0xffffffc0, v186
	v_or_b32_e32 v25, v25, v27
	v_lshrrev_b32_e32 v26, 6, v186
	v_lshrrev_b32_e32 v27, 6, v185
	v_lshl_add_u32 v26, v26, 2, v27
	v_mul_u32_u24_e32 v26, 0x900, v26
	v_add_u32_e32 v26, 0x21800, v26
	v_add_u32_e32 v191, v191, v26
	v_and_b32_e32 v27, 15, v186
	v_mul_u32_u24_e32 v190, 0x90, v27
	v_bfe_u32 v27, v185, 4, 2
	v_lshl_add_u32 v190, v27, 5, v190
	v_add_u32_e32 v190, v190, v26
	v_lshl_add_u64 v[250:251], v[192:193], 2, s[18:19]
	s_mov_b32 s101, 0
	global_load_dwordx4 v[206:209], v[250:251], off offset:48
	global_load_dwordx4 v[210:213], v[250:251], off offset:32
	global_load_dwordx4 v[214:217], v[250:251], off offset:16
	global_load_dwordx4 v[218:221], v[250:251], off
	s_mov_b32 s100, 0x10000
	v_lshl_add_u64 v[234:235], v[250:251], 0, s[100:101]
	global_load_dwordx4 v[222:225], v[234:235], off offset:48
	global_load_dwordx4 v[226:229], v[234:235], off offset:32
	global_load_dwordx4 v[230:233], v[234:235], off offset:16
	s_nop 0
	global_load_dwordx4 v[234:237], v[234:235], off
	s_mov_b32 s100, 0x20000
	v_lshl_add_u64 v[192:193], v[250:251], 0, s[100:101]
	global_load_dwordx4 v[238:241], v[192:193], off offset:48
	global_load_dwordx4 v[242:245], v[192:193], off offset:32
	global_load_dwordx4 v[246:249], v[192:193], off offset:16
	s_nop 0
	global_load_dwordx4 v[192:195], v[192:193], off
	s_waitcnt vmcnt(12)
	v_pk_mul_f32 v[12:13], v[2:3], s[84:85] op_sel_hi:[1,0]
	v_pk_mul_f32 v[2:3], v[18:19], s[84:85] op_sel_hi:[1,0]
	v_lshl_add_u32 v18, s65, 8, v25
	v_ashrrev_i32_e32 v19, 31, v18
	v_pk_mul_f32 v[14:15], v[0:1], s[84:85] op_sel_hi:[1,0]
	v_pk_mul_f32 v[0:1], v[20:21], s[84:85] op_sel_hi:[1,0]
	v_lshlrev_b64 v[20:21], 10, v[18:19]
	v_lshl_add_u64 v[26:27], v[20:21], 0, v[16:17]
	v_pk_mul_f32 v[8:9], v[6:7], s[84:85] op_sel_hi:[1,0]
	v_pk_mul_f32 v[10:11], v[4:5], s[84:85] op_sel_hi:[1,0]
	v_pk_mul_f32 v[4:5], v[176:177], s[84:85] op_sel_hi:[1,0]
	v_pk_mul_f32 v[6:7], v[174:175], s[84:85] op_sel_hi:[1,0]
	v_lshl_add_u64 v[26:27], v[26:27], 1, s[50:51]
	s_waitcnt vmcnt(11)
	v_pk_mul_f32 v[22:23], v[208:209], s[86:87] op_sel_hi:[1,0]
	v_pk_mul_f32 v[20:21], v[206:207], s[86:87] op_sel_hi:[1,0]
	s_waitcnt vmcnt(9)
	v_pk_mul_f32 v[180:181], v[216:217], s[86:87] op_sel_hi:[1,0]
	v_pk_mul_f32 v[178:179], v[214:215], s[86:87] op_sel_hi:[1,0]
	s_waitcnt vmcnt(8)
	v_pk_mul_f32 v[182:183], v[220:221], s[86:87] op_sel_hi:[1,0]
	v_pk_mul_f32 v[188:189], v[218:219], s[86:87] op_sel_hi:[1,0]
	v_pk_fma_f32 v[180:181], v[146:147], v[8:9], v[180:181]
	v_pk_fma_f32 v[146:147], v[144:145], v[10:11], v[178:179]
	v_pk_fma_f32 v[154:155], v[154:155], v[12:13], v[182:183]
	v_pk_fma_f32 v[152:153], v[152:153], v[14:15], v[188:189]
	v_pk_fma_f32 v[150:151], v[150:151], v[0:1], v[22:23]
	v_cvt_pk_bf16_f32 v144, v152, v153
	v_cvt_pk_bf16_f32 v145, v154, v155
	v_cvt_pk_bf16_f32 v146, v146, v147
	v_cvt_pk_bf16_f32 v147, v180, v181
	ds_write_b128 v190, v[144:147]
	v_pk_fma_f32 v[22:23], v[148:149], v[2:3], v[20:21]
	s_nop 0
	v_pk_mul_f32 v[146:147], v[210:211], s[86:87] op_sel_hi:[1,0]
	v_pk_mul_f32 v[144:145], v[212:213], s[86:87] op_sel_hi:[1,0]
	v_pk_fma_f32 v[146:147], v[156:157], v[6:7], v[146:147]
	v_pk_fma_f32 v[144:145], v[158:159], v[4:5], v[144:145]
	v_cvt_pk_bf16_f32 v20, v146, v147
	s_nop 0
	v_cvt_pk_bf16_f32 v21, v144, v145
	v_cvt_pk_bf16_f32 v22, v22, v23
	v_cvt_pk_bf16_f32 v23, v150, v151
	ds_write_b128 v190, v[20:23] offset:16
	ds_read_b128 v[144:147], v191
	ds_read_b128 v[20:23], v191 offset:1152
	s_mov_b32 s100, 0x4000
	v_lshl_add_u64 v[188:189], v[26:27], 0, s[100:101]
	s_waitcnt lgkmcnt(0)
	global_store_dwordx4 v[26:27], v[144:147], off
	global_store_dwordx4 v[188:189], v[20:23], off
	s_nop 1
	v_or_b32_e32 v20, 16, v18
	v_ashrrev_i32_e32 v21, 31, v20
	v_lshlrev_b64 v[20:21], 10, v[20:21]
	v_lshl_add_u64 v[26:27], v[20:21], 0, v[16:17]
	s_mov_b32 s100, 0x30000
	v_lshl_add_u64 v[218:219], v[250:251], 0, s[100:101]
	global_load_dwordx4 v[206:209], v[218:219], off offset:48
	global_load_dwordx4 v[210:213], v[218:219], off offset:32
	global_load_dwordx4 v[214:217], v[218:219], off offset:16
	s_nop 0
	global_load_dwordx4 v[218:221], v[218:219], off
	v_lshl_add_u64 v[26:27], v[26:27], 1, s[50:51]
	s_waitcnt vmcnt(13)
	v_pk_mul_f32 v[22:23], v[224:225], s[86:87] op_sel_hi:[1,0]
	v_pk_mul_f32 v[20:21], v[222:223], s[86:87] op_sel_hi:[1,0]
	s_waitcnt vmcnt(11)
	v_pk_mul_f32 v[150:151], v[232:233], s[86:87] op_sel_hi:[1,0]
	v_pk_mul_f32 v[148:149], v[230:231], s[86:87] op_sel_hi:[1,0]
	s_waitcnt vmcnt(10)
; __device__ __forceinline__ unsigned cvt_pk_bf16(float lo, float hi) { unsigned r; asm volatile("v_cvt_pk_bf16_f32 %0, %1, %2" : "=v"(r) : "v"(lo), "v"(hi)); return r; }
;     __device__ __forceinline__ void operator()(const f32x4 (&acc)[2][2][4][2], const Unit& u, int wr, int wc, int fr, int fq, const LAS unsigned* rt) const {
;     ...
;         for (int ai = 0; ai < 2; ++ai)
; #pragma unroll
;             for (int m = 0; m < 4; ++m) { const size_t o = (size_t)(u.pm * BM + ai * HALF + wr * 64 + m * 16 + fr) * D + col0;
;                 const f32x4 x0 = *(const f32x4*)(x + o), x1 = *(const f32x4*)(x + o + 4), x2 = *(const f32x4*)(x + o + 8), x3 = *(const f32x4*)(x + o + 12);
;                 const f32x4 xs[2][2] = {{x0, x1}, {x2, x3}};
; #pragma unroll
;                 for (int bj = 0; bj < 2; ++bj) {
;                     const f32x4 t0 = xs[bj][0] * ALPHA + g[bj][0] * acc[ai][bj][m][0], t1 = xs[bj][1] * ALPHA + g[bj][1] * acc[ai][bj][m][1];
;                     u32x4 w; w.x = cvt_pk_bf16(t0[0], t0[1]); w.y = cvt_pk_bf16(t0[2], t0[3]); w.z = cvt_pk_bf16(t1[0], t1[1]); w.w = cvt_pk_bf16(t1[2], t1[3]);
;                     *(u32x4*)(tb + o + 8 * bj) = w; } }
	v_pk_mul_f32 v[154:155], v[236:237], s[86:87] op_sel_hi:[1,0]
	v_pk_mul_f32 v[152:153], v[234:235], s[86:87] op_sel_hi:[1,0]
	v_pk_fma_f32 v[150:151], v[130:131], v[8:9], v[150:151]
	v_pk_fma_f32 v[130:131], v[128:129], v[10:11], v[148:149]
	v_pk_fma_f32 v[138:139], v[138:139], v[12:13], v[154:155]
	v_pk_fma_f32 v[136:137], v[136:137], v[14:15], v[152:153]
	v_pk_fma_f32 v[134:135], v[134:135], v[0:1], v[22:23]
	v_cvt_pk_bf16_f32 v128, v136, v137
	v_cvt_pk_bf16_f32 v129, v138, v139
	v_cvt_pk_bf16_f32 v130, v130, v131
	v_cvt_pk_bf16_f32 v131, v150, v151
	ds_write_b128 v190, v[128:131]
	v_pk_fma_f32 v[22:23], v[132:133], v[2:3], v[20:21]
	s_nop 0
	v_pk_mul_f32 v[130:131], v[226:227], s[86:87] op_sel_hi:[1,0]
	v_pk_mul_f32 v[128:129], v[228:229], s[86:87] op_sel_hi:[1,0]
	v_pk_fma_f32 v[130:131], v[140:141], v[6:7], v[130:131]
	v_pk_fma_f32 v[128:129], v[142:143], v[4:5], v[128:129]
	v_cvt_pk_bf16_f32 v20, v130, v131
	s_nop 0
	v_cvt_pk_bf16_f32 v21, v128, v129
	v_cvt_pk_bf16_f32 v22, v22, v23
	v_cvt_pk_bf16_f32 v23, v134, v135
	ds_write_b128 v190, v[20:23] offset:16
	ds_read_b128 v[128:131], v191
	ds_read_b128 v[20:23], v191 offset:1152
	s_mov_b32 s100, 0x4000
	v_lshl_add_u64 v[188:189], v[26:27], 0, s[100:101]
	s_waitcnt lgkmcnt(0)
	global_store_dwordx4 v[26:27], v[128:131], off
	global_store_dwordx4 v[188:189], v[20:23], off
	s_nop 1
	v_or_b32_e32 v20, 32, v18
	v_ashrrev_i32_e32 v21, 31, v20
	v_lshlrev_b64 v[20:21], 10, v[20:21]
	v_lshl_add_u64 v[26:27], v[20:21], 0, v[16:17]
	s_mov_b32 s100, 0x80000
	v_lshl_add_u64 v[234:235], v[250:251], 0, s[100:101]
	global_load_dwordx4 v[222:225], v[234:235], off offset:48
	global_load_dwordx4 v[226:229], v[234:235], off offset:32
	global_load_dwordx4 v[230:233], v[234:235], off offset:16
	s_nop 0
	global_load_dwordx4 v[234:237], v[234:235], off
	v_lshl_add_u64 v[26:27], v[26:27], 1, s[50:51]
	s_waitcnt vmcnt(15)
	v_pk_mul_f32 v[22:23], v[240:241], s[86:87] op_sel_hi:[1,0]
	v_pk_mul_f32 v[20:21], v[238:239], s[86:87] op_sel_hi:[1,0]
	s_waitcnt vmcnt(13)
	v_pk_mul_f32 v[134:135], v[248:249], s[86:87] op_sel_hi:[1,0]
	v_pk_mul_f32 v[132:133], v[246:247], s[86:87] op_sel_hi:[1,0]
	s_waitcnt vmcnt(12)
	v_pk_mul_f32 v[138:139], v[194:195], s[86:87] op_sel_hi:[1,0]
	v_pk_mul_f32 v[136:137], v[192:193], s[86:87] op_sel_hi:[1,0]
	v_pk_fma_f32 v[134:135], v[114:115], v[8:9], v[134:135]
	v_pk_fma_f32 v[114:115], v[112:113], v[10:11], v[132:133]
	v_pk_fma_f32 v[122:123], v[122:123], v[12:13], v[138:139]
	v_pk_fma_f32 v[120:121], v[120:121], v[14:15], v[136:137]
	v_pk_fma_f32 v[118:119], v[118:119], v[0:1], v[22:23]
	v_cvt_pk_bf16_f32 v112, v120, v121
	v_cvt_pk_bf16_f32 v113, v122, v123
	v_cvt_pk_bf16_f32 v114, v114, v115
	v_cvt_pk_bf16_f32 v115, v134, v135
	ds_write_b128 v190, v[112:115]
	v_pk_fma_f32 v[22:23], v[116:117], v[2:3], v[20:21]
	s_nop 0
	v_pk_mul_f32 v[114:115], v[242:243], s[86:87] op_sel_hi:[1,0]
	v_pk_mul_f32 v[112:113], v[244:245], s[86:87] op_sel_hi:[1,0]
	v_pk_fma_f32 v[114:115], v[124:125], v[6:7], v[114:115]
	v_pk_fma_f32 v[112:113], v[126:127], v[4:5], v[112:113]
	v_cvt_pk_bf16_f32 v20, v114, v115
	s_nop 0
	v_cvt_pk_bf16_f32 v21, v112, v113
	v_cvt_pk_bf16_f32 v22, v22, v23
	v_cvt_pk_bf16_f32 v23, v118, v119
	ds_write_b128 v190, v[20:23] offset:16
	ds_read_b128 v[112:115], v191
	ds_read_b128 v[20:23], v191 offset:1152
	s_mov_b32 s100, 0x4000
	v_lshl_add_u64 v[188:189], v[26:27], 0, s[100:101]
	s_waitcnt lgkmcnt(0)
	global_store_dwordx4 v[26:27], v[112:115], off
	global_store_dwordx4 v[188:189], v[20:23], off
	s_nop 1
	v_or_b32_e32 v20, 48, v18
	v_ashrrev_i32_e32 v21, 31, v20
	v_lshlrev_b64 v[20:21], 10, v[20:21]
	v_lshl_add_u64 v[26:27], v[20:21], 0, v[16:17]
	s_mov_b32 s100, 0x90000
	v_lshl_add_u64 v[192:193], v[250:251], 0, s[100:101]
	global_load_dwordx4 v[238:241], v[192:193], off offset:48
	global_load_dwordx4 v[242:245], v[192:193], off offset:32
	global_load_dwordx4 v[246:249], v[192:193], off offset:16
	s_nop 0
	global_load_dwordx4 v[192:195], v[192:193], off
	v_lshl_add_u64 v[26:27], v[26:27], 1, s[50:51]
	s_waitcnt vmcnt(15)
	v_pk_mul_f32 v[22:23], v[208:209], s[86:87] op_sel_hi:[1,0]
	v_pk_mul_f32 v[20:21], v[206:207], s[86:87] op_sel_hi:[1,0]
	s_waitcnt vmcnt(13)
	v_pk_mul_f32 v[118:119], v[216:217], s[86:87] op_sel_hi:[1,0]
	v_pk_mul_f32 v[116:117], v[214:215], s[86:87] op_sel_hi:[1,0]
	s_waitcnt vmcnt(12)
	v_pk_mul_f32 v[122:123], v[220:221], s[86:87] op_sel_hi:[1,0]
	v_pk_mul_f32 v[120:121], v[218:219], s[86:87] op_sel_hi:[1,0]
	v_pk_fma_f32 v[118:119], v[98:99], v[8:9], v[118:119]
	v_pk_fma_f32 v[98:99], v[96:97], v[10:11], v[116:117]
	v_pk_fma_f32 v[106:107], v[106:107], v[12:13], v[122:123]
	v_pk_fma_f32 v[104:105], v[104:105], v[14:15], v[120:121]
	v_pk_fma_f32 v[102:103], v[102:103], v[0:1], v[22:23]
	v_cvt_pk_bf16_f32 v96, v104, v105
	v_cvt_pk_bf16_f32 v97, v106, v107
	v_cvt_pk_bf16_f32 v98, v98, v99
	v_cvt_pk_bf16_f32 v99, v118, v119
	ds_write_b128 v190, v[96:99]
	v_pk_fma_f32 v[22:23], v[100:101], v[2:3], v[20:21]
	s_nop 0
	v_pk_mul_f32 v[98:99], v[210:211], s[86:87] op_sel_hi:[1,0]
	v_pk_mul_f32 v[96:97], v[212:213], s[86:87] op_sel_hi:[1,0]
	v_pk_fma_f32 v[98:99], v[108:109], v[6:7], v[98:99]
	v_pk_fma_f32 v[96:97], v[110:111], v[4:5], v[96:97]
	v_cvt_pk_bf16_f32 v20, v98, v99
	s_nop 0
	v_cvt_pk_bf16_f32 v21, v96, v97
	v_cvt_pk_bf16_f32 v22, v22, v23
	v_cvt_pk_bf16_f32 v23, v102, v103
	ds_write_b128 v190, v[20:23] offset:16
	ds_read_b128 v[96:99], v191
	ds_read_b128 v[20:23], v191 offset:1152
	s_mov_b32 s100, 0x4000
	v_lshl_add_u64 v[188:189], v[26:27], 0, s[100:101]
	s_waitcnt lgkmcnt(0)
; __device__ __forceinline__ unsigned cvt_pk_bf16(float lo, float hi) { unsigned r; asm volatile("v_cvt_pk_bf16_f32 %0, %1, %2" : "=v"(r) : "v"(lo), "v"(hi)); return r; }
;     __device__ __forceinline__ void operator()(const f32x4 (&acc)[2][2][4][2], const Unit& u, int wr, int wc, int fr, int fq, const LAS unsigned* rt) const {
;     ...
;         for (int ai = 0; ai < 2; ++ai)
; #pragma unroll
;             for (int m = 0; m < 4; ++m) { const size_t o = (size_t)(u.pm * BM + ai * HALF + wr * 64 + m * 16 + fr) * D + col0;
;                 const f32x4 x0 = *(const f32x4*)(x + o), x1 = *(const f32x4*)(x + o + 4), x2 = *(const f32x4*)(x + o + 8), x3 = *(const f32x4*)(x + o + 12);
;                 const f32x4 xs[2][2] = {{x0, x1}, {x2, x3}};
; #pragma unroll
;                 for (int bj = 0; bj < 2; ++bj) {
;                     const f32x4 t0 = xs[bj][0] * ALPHA + g[bj][0] * acc[ai][bj][m][0], t1 = xs[bj][1] * ALPHA + g[bj][1] * acc[ai][bj][m][1];
;                     u32x4 w; w.x = cvt_pk_bf16(t0[0], t0[1]); w.y = cvt_pk_bf16(t0[2], t0[3]); w.z = cvt_pk_bf16(t1[0], t1[1]); w.w = cvt_pk_bf16(t1[2], t1[3]);
;                     *(u32x4*)(tb + o + 8 * bj) = w; } }
	global_store_dwordx4 v[26:27], v[96:99], off
	global_store_dwordx4 v[188:189], v[20:23], off
	s_nop 1
	v_add_u32_e32 v20, 0x80, v18
	v_ashrrev_i32_e32 v21, 31, v20
	v_lshlrev_b64 v[20:21], 10, v[20:21]
	v_lshl_add_u64 v[26:27], v[20:21], 0, v[16:17]
	s_mov_b32 s100, 0xa0000
	v_lshl_add_u64 v[218:219], v[250:251], 0, s[100:101]
	global_load_dwordx4 v[206:209], v[218:219], off offset:48
	global_load_dwordx4 v[210:213], v[218:219], off offset:32
	global_load_dwordx4 v[214:217], v[218:219], off offset:16
	s_nop 0
	global_load_dwordx4 v[218:221], v[218:219], off
	v_lshl_add_u64 v[26:27], v[26:27], 1, s[50:51]
	s_waitcnt vmcnt(15)
	v_pk_mul_f32 v[22:23], v[224:225], s[86:87] op_sel_hi:[1,0]
	v_pk_mul_f32 v[20:21], v[222:223], s[86:87] op_sel_hi:[1,0]
	s_waitcnt vmcnt(13)
	v_pk_mul_f32 v[102:103], v[232:233], s[86:87] op_sel_hi:[1,0]
	v_pk_mul_f32 v[100:101], v[230:231], s[86:87] op_sel_hi:[1,0]
	s_waitcnt vmcnt(12)
	v_pk_mul_f32 v[106:107], v[236:237], s[86:87] op_sel_hi:[1,0]
	v_pk_mul_f32 v[104:105], v[234:235], s[86:87] op_sel_hi:[1,0]
	v_pk_fma_f32 v[102:103], v[82:83], v[8:9], v[102:103]
	v_pk_fma_f32 v[82:83], v[80:81], v[10:11], v[100:101]
	v_pk_fma_f32 v[90:91], v[90:91], v[12:13], v[106:107]
	v_pk_fma_f32 v[88:89], v[88:89], v[14:15], v[104:105]
	v_pk_fma_f32 v[86:87], v[86:87], v[0:1], v[22:23]
	v_cvt_pk_bf16_f32 v80, v88, v89
	v_cvt_pk_bf16_f32 v81, v90, v91
	v_cvt_pk_bf16_f32 v82, v82, v83
	v_cvt_pk_bf16_f32 v83, v102, v103
	ds_write_b128 v190, v[80:83]
	v_pk_fma_f32 v[22:23], v[84:85], v[2:3], v[20:21]
	s_nop 0
	v_pk_mul_f32 v[82:83], v[226:227], s[86:87] op_sel_hi:[1,0]
	v_pk_mul_f32 v[80:81], v[228:229], s[86:87] op_sel_hi:[1,0]
	v_pk_fma_f32 v[82:83], v[92:93], v[6:7], v[82:83]
	v_pk_fma_f32 v[80:81], v[94:95], v[4:5], v[80:81]
	v_cvt_pk_bf16_f32 v20, v82, v83
	s_nop 0
	v_cvt_pk_bf16_f32 v21, v80, v81
	v_cvt_pk_bf16_f32 v22, v22, v23
	v_cvt_pk_bf16_f32 v23, v86, v87
	ds_write_b128 v190, v[20:23] offset:16
	ds_read_b128 v[80:83], v191
	ds_read_b128 v[20:23], v191 offset:1152
	s_mov_b32 s100, 0x4000
	v_lshl_add_u64 v[188:189], v[26:27], 0, s[100:101]
	s_waitcnt lgkmcnt(0)
	global_store_dwordx4 v[26:27], v[80:83], off
	global_store_dwordx4 v[188:189], v[20:23], off
	s_nop 1
	v_add_u32_e32 v20, 0x90, v18
	v_ashrrev_i32_e32 v21, 31, v20
	v_lshlrev_b64 v[20:21], 10, v[20:21]
	v_lshl_add_u64 v[26:27], v[20:21], 0, v[16:17]
	s_mov_b32 s100, 0xb0000
	v_lshl_add_u64 v[234:235], v[250:251], 0, s[100:101]
	global_load_dwordx4 v[222:225], v[234:235], off offset:48
	global_load_dwordx4 v[226:229], v[234:235], off offset:32
	global_load_dwordx4 v[230:233], v[234:235], off offset:16
	s_nop 0
	global_load_dwordx4 v[234:237], v[234:235], off
	v_lshl_add_u64 v[26:27], v[26:27], 1, s[50:51]
	s_waitcnt vmcnt(15)
	v_pk_mul_f32 v[22:23], v[240:241], s[86:87] op_sel_hi:[1,0]
	v_pk_mul_f32 v[20:21], v[238:239], s[86:87] op_sel_hi:[1,0]
	s_waitcnt vmcnt(13)
	v_pk_mul_f32 v[86:87], v[248:249], s[86:87] op_sel_hi:[1,0]
	v_pk_mul_f32 v[84:85], v[246:247], s[86:87] op_sel_hi:[1,0]
	s_waitcnt vmcnt(12)
	v_pk_mul_f32 v[90:91], v[194:195], s[86:87] op_sel_hi:[1,0]
	v_pk_mul_f32 v[88:89], v[192:193], s[86:87] op_sel_hi:[1,0]
	v_pk_fma_f32 v[86:87], v[66:67], v[8:9], v[86:87]
	v_pk_fma_f32 v[66:67], v[64:65], v[10:11], v[84:85]
	v_pk_fma_f32 v[74:75], v[74:75], v[12:13], v[90:91]
	v_pk_fma_f32 v[72:73], v[72:73], v[14:15], v[88:89]
	v_pk_fma_f32 v[70:71], v[70:71], v[0:1], v[22:23]
	v_cvt_pk_bf16_f32 v64, v72, v73
	v_cvt_pk_bf16_f32 v65, v74, v75
	v_cvt_pk_bf16_f32 v66, v66, v67
	v_cvt_pk_bf16_f32 v67, v86, v87
	ds_write_b128 v190, v[64:67]
	v_pk_fma_f32 v[22:23], v[68:69], v[2:3], v[20:21]
	s_nop 0
	v_pk_mul_f32 v[66:67], v[242:243], s[86:87] op_sel_hi:[1,0]
	v_pk_mul_f32 v[64:65], v[244:245], s[86:87] op_sel_hi:[1,0]
	v_pk_fma_f32 v[66:67], v[76:77], v[6:7], v[66:67]
	v_pk_fma_f32 v[64:65], v[78:79], v[4:5], v[64:65]
	v_cvt_pk_bf16_f32 v20, v66, v67
	s_nop 0
	v_cvt_pk_bf16_f32 v21, v64, v65
	v_cvt_pk_bf16_f32 v22, v22, v23
	v_cvt_pk_bf16_f32 v23, v70, v71
	ds_write_b128 v190, v[20:23] offset:16
	ds_read_b128 v[64:67], v191
	ds_read_b128 v[20:23], v191 offset:1152
	s_mov_b32 s100, 0x4000
	v_lshl_add_u64 v[188:189], v[26:27], 0, s[100:101]
	s_waitcnt lgkmcnt(0)
; #define LAS __attribute__((address_space(3)))
; __device__ __forceinline__ unsigned cvt_pk_bf16(float lo, float hi) { unsigned r; asm volatile("v_cvt_pk_bf16_f32 %0, %1, %2" : "=v"(r) : "v"(lo), "v"(hi)); return r; }
; __device__ __forceinline__ int lane_id() { return (int)__builtin_amdgcn_mbcnt_hi(~0u, __builtin_amdgcn_mbcnt_lo(~0u, 0u)); }
; #define PG8_BAR __builtin_amdgcn_s_barrier()
;     ...
;         { const int l2 = lane_id(); E(acc, cur, wr, wc, l2 & 15, l2 >> 4, rowtab + 512 * (ui % 3)); }
;         if (!has_next) break;
; #pragma unroll
;         for (int a = 0; a < 2; ++a)
; #pragma unroll
;             for (int b = 0; b < 2; ++b)
; #pragma unroll
;                 for (int m = 0; m < 4; ++m)
; #pragma unroll
;                     for (int n = 0; n < 2; ++n) acc[a][b][m][n] = (f32x4){0.f, 0.f, 0.f, 0.f};
;         cur = nxt; cB = nB; cA = nA; ++ui; fresh_cur = fresh_nxt;
;         if constexpr (GATHER) { const u32x4 _t = *(const LAS u32x4*)vnslot; vc[0][0] = _t.x; vc[0][1] = _t.y; vc[1][0] = _t.z; vc[1][1] = _t.w; }
;         if (wr == 1) PG8_BAR;
;     __device__ __forceinline__ void operator()(const f32x4 (&acc)[2][2][4][2], const Unit& u, int wr, int wc, int fr, int fq, const LAS unsigned* rt) const {
;     ...
;         for (int ai = 0; ai < 2; ++ai)
; #pragma unroll
;             for (int m = 0; m < 4; ++m) { const size_t o = (size_t)(u.pm * BM + ai * HALF + wr * 64 + m * 16 + fr) * D + col0;
;                 const f32x4 x0 = *(const f32x4*)(x + o), x1 = *(const f32x4*)(x + o + 4), x2 = *(const f32x4*)(x + o + 8), x3 = *(const f32x4*)(x + o + 12);
;                 const f32x4 xs[2][2] = {{x0, x1}, {x2, x3}};
; #pragma unroll
;                 for (int bj = 0; bj < 2; ++bj) {
;                     const f32x4 t0 = xs[bj][0] * ALPHA + g[bj][0] * acc[ai][bj][m][0], t1 = xs[bj][1] * ALPHA + g[bj][1] * acc[ai][bj][m][1];
;                     u32x4 w; w.x = cvt_pk_bf16(t0[0], t0[1]); w.y = cvt_pk_bf16(t0[2], t0[3]); w.z = cvt_pk_bf16(t1[0], t1[1]); w.w = cvt_pk_bf16(t1[2], t1[3]);
;                     *(u32x4*)(tb + o + 8 * bj) = w; } }
;     }
	global_store_dwordx4 v[26:27], v[64:67], off
	global_store_dwordx4 v[188:189], v[20:23], off
	s_nop 1
	v_add_u32_e32 v20, 0xa0, v18
	v_ashrrev_i32_e32 v21, 31, v20
	v_lshlrev_b64 v[20:21], 10, v[20:21]
	v_lshl_add_u64 v[26:27], v[20:21], 0, v[16:17]
	v_add_u32_e32 v18, 0xb0, v18
	v_lshl_add_u64 v[26:27], v[26:27], 1, s[50:51]
	v_ashrrev_i32_e32 v19, 31, v18
	v_lshlrev_b64 v[18:19], 10, v[18:19]
	s_waitcnt vmcnt(11)
	v_pk_mul_f32 v[22:23], v[208:209], s[86:87] op_sel_hi:[1,0]
	v_pk_mul_f32 v[20:21], v[206:207], s[86:87] op_sel_hi:[1,0]
	s_waitcnt vmcnt(9)
	v_pk_mul_f32 v[70:71], v[216:217], s[86:87] op_sel_hi:[1,0]
	v_pk_mul_f32 v[68:69], v[214:215], s[86:87] op_sel_hi:[1,0]
	s_waitcnt vmcnt(8)
	v_pk_mul_f32 v[74:75], v[220:221], s[86:87] op_sel_hi:[1,0]
	v_pk_mul_f32 v[72:73], v[218:219], s[86:87] op_sel_hi:[1,0]
	v_pk_fma_f32 v[70:71], v[50:51], v[8:9], v[70:71]
	v_pk_fma_f32 v[50:51], v[48:49], v[10:11], v[68:69]
	v_pk_fma_f32 v[58:59], v[58:59], v[12:13], v[74:75]
	v_pk_fma_f32 v[56:57], v[56:57], v[14:15], v[72:73]
	v_pk_fma_f32 v[54:55], v[54:55], v[0:1], v[22:23]
	v_cvt_pk_bf16_f32 v48, v56, v57
	v_cvt_pk_bf16_f32 v49, v58, v59
	v_cvt_pk_bf16_f32 v50, v50, v51
	v_cvt_pk_bf16_f32 v51, v70, v71
	ds_write_b128 v190, v[48:51]
	v_pk_fma_f32 v[22:23], v[52:53], v[2:3], v[20:21]
	s_nop 0
	v_pk_mul_f32 v[48:49], v[212:213], s[86:87] op_sel_hi:[1,0]
	v_pk_mul_f32 v[50:51], v[210:211], s[86:87] op_sel_hi:[1,0]
	v_pk_fma_f32 v[48:49], v[62:63], v[4:5], v[48:49]
	v_pk_fma_f32 v[50:51], v[60:61], v[6:7], v[50:51]
	s_nop 0
	v_cvt_pk_bf16_f32 v20, v50, v51
	v_cvt_pk_bf16_f32 v21, v48, v49
	v_cvt_pk_bf16_f32 v22, v22, v23
	v_cvt_pk_bf16_f32 v23, v54, v55
	ds_write_b128 v190, v[20:23] offset:16
	ds_read_b128 v[48:51], v191
	ds_read_b128 v[20:23], v191 offset:1152
	s_mov_b32 s100, 0x4000
	v_lshl_add_u64 v[188:189], v[26:27], 0, s[100:101]
	s_waitcnt lgkmcnt(0)
	global_store_dwordx4 v[26:27], v[48:51], off
	global_store_dwordx4 v[188:189], v[20:23], off
	v_lshl_add_u64 v[26:27], v[18:19], 0, v[16:17]
	s_waitcnt vmcnt(4)
	v_pk_mul_f32 v[54:55], v[236:237], s[86:87] op_sel_hi:[1,0]
	v_pk_mul_f32 v[52:53], v[234:235], s[86:87] op_sel_hi:[1,0]
	v_pk_fma_f32 v[12:13], v[46:47], v[12:13], v[54:55]
	v_pk_mul_f32 v[46:47], v[230:231], s[86:87] op_sel_hi:[1,0]
	v_pk_fma_f32 v[14:15], v[44:45], v[14:15], v[52:53]
	v_pk_mul_f32 v[44:45], v[232:233], s[86:87] op_sel_hi:[1,0]
	v_pk_fma_f32 v[10:11], v[40:41], v[10:11], v[46:47]
	v_pk_fma_f32 v[42:43], v[42:43], v[8:9], v[44:45]
	v_cvt_pk_bf16_f32 v8, v14, v15
	v_cvt_pk_bf16_f32 v9, v12, v13
	v_cvt_pk_bf16_f32 v10, v10, v11
	v_lshl_add_u64 v[12:13], v[26:27], 1, s[50:51]
	v_cvt_pk_bf16_f32 v11, v42, v43
	ds_write_b128 v190, v[8:11]
	s_nop 1
	v_pk_mul_f32 v[10:11], v[226:227], s[86:87] op_sel_hi:[1,0]
	v_pk_mul_f32 v[8:9], v[228:229], s[86:87] op_sel_hi:[1,0]
	v_pk_fma_f32 v[6:7], v[36:37], v[6:7], v[10:11]
	v_pk_mul_f32 v[10:11], v[222:223], s[86:87] op_sel_hi:[1,0]
	v_pk_fma_f32 v[4:5], v[38:39], v[4:5], v[8:9]
	v_pk_mul_f32 v[8:9], v[224:225], s[86:87] op_sel_hi:[1,0]
	v_pk_fma_f32 v[2:3], v[32:33], v[2:3], v[10:11]
	v_pk_fma_f32 v[8:9], v[34:35], v[0:1], v[8:9]
	v_cvt_pk_bf16_f32 v0, v6, v7
	v_cvt_pk_bf16_f32 v1, v4, v5
	v_cvt_pk_bf16_f32 v2, v2, v3
	s_nop 0
	v_cvt_pk_bf16_f32 v3, v8, v9
	ds_write_b128 v190, v[0:3] offset:16
	ds_read_b128 v[8:11], v191
	ds_read_b128 v[0:3], v191 offset:1152
	s_mov_b32 s100, 0x4000
	v_lshl_add_u64 v[188:189], v[12:13], 0, s[100:101]
	s_waitcnt lgkmcnt(0)
	global_store_dwordx4 v[12:13], v[8:11], off
	global_store_dwordx4 v[188:189], v[0:3], off
	s_cbranch_scc1 .LBB0_404
	s_and_b64 s[4:5], s[8:9], exec
	s_cselect_b32 s12, s64, s12
	s_andn2_b64 vcc, exec, s[10:11]
	s_cbranch_vccnz .LBB0_403
	s_barrier
	s_branch .LBB0_403
